# EpiThin: second-half residual rows prefetched during first-half compute into dead registers (no vmcnt(0) drain at the half boundary)
# baseline (speedup 1.0000x reference)
; __device__ __forceinline__ unsigned cvt_pk_bf16(float lo, float hi) { unsigned r; asm volatile("v_cvt_pk_bf16_f32 %0, %1, %2" : "=v"(r) : "v"(lo), "v"(hi)); return r; }
; __device__ __forceinline__ float epi_xor16(float v) { return __builtin_bit_cast(float, __builtin_amdgcn_ds_swizzle(__builtin_bit_cast(int, v), (16 << 10) | 0x1f)); }
;     __device__ __forceinline__ void operator()(const f32x4 (&acc)[2][2][4][2], const Unit& u, int wr, int wc, int fr, int fq) const {
;     ...
;             if (ai == 1) {
; #pragma unroll
;                 for (int m = 0; m < 4; ++m)
; #pragma unroll
;                     for (int bj = 0; bj < 2; ++bj) xa[m][bj] = *(const u32x4*)(XB + (size_t)(row0 + HALF + m * 16) * 1024 + col0 + bj * HALF); }
; #pragma unroll
;             for (int m = 0; m < 4; ++m) { const int row = row0 + ai * HALF + m * 16; const float rF = scr[1024 + (row & 255)]; f32x2 s2p = {0.f, 0.f};
; #pragma unroll
;                 for (int bj = 0; bj < 2; ++bj) { const u32x4 xw = xa[m][bj]; float o[8];
; #pragma unroll
;                     for (int n = 0; n < 2; ++n)
; #pragma unroll
;                         for (int e = 0; e < 4; e += 2) { const int q = n * 4 + e; const unsigned w = xw[q >> 1];
;                             const f32x2 xv = {__builtin_bit_cast(float, w << 16), __builtin_bit_cast(float, w & 0xffff0000u)}, av = {acc[ai][bj][m][n][e], acc[ai][bj][m][n][e + 1]}, gv = {gp[bj][q], gp[bj][q + 1]};
;                             const f32x2 ov = xv + av * (gv * rF); s2p += ov * ov; o[q] = ov[0]; o[q + 1] = ov[1]; }
;                     if (OUT) { float* op = OUT + (size_t)row * 1024 + col0 + bj * HALF;
;                         __builtin_nontemporal_store((f32x4){o[0], o[1], o[2], o[3]}, (f32x4*)op); __builtin_nontemporal_store((f32x4){o[4], o[5], o[6], o[7]}, (f32x4*)(op + 4)); }
;                     else { u32x4 w; w.x = cvt_pk_bf16(o[0], o[1]); w.y = cvt_pk_bf16(o[2], o[3]); w.z = cvt_pk_bf16(o[4], o[5]); w.w = cvt_pk_bf16(o[6], o[7]);
;                         *(u32x4*)(XB + (size_t)row * 1024 + col0 + bj * HALF) = w; } }
;                 float s2 = s2p[0] + s2p[1];
;                 s2 += epi_xor16(s2); s2 += epi_xor32(s2, lane);
;                 if (fq == 0) scr[wc * 256 + (row & 255)] = s2; }
.LBB0_618:
	v_add_u32_e32 v200, 0x80, v196
	v_ashrrev_i32_e32 v201, 31, v200
	v_lshlrev_b64 v[200:201], 11, v[200:201]
	v_lshl_add_u64 v[200:201], v[198:199], 0, v[200:201]
	global_load_dwordx4 v[200:203], v[200:201], off
	v_add_u32_e32 v246, 0x80, v196
	v_ashrrev_i32_e32 v247, 31, v246
	v_lshlrev_b64 v[246:247], 11, v[246:247]
	v_lshl_add_u64 v[246:247], v[198:199], 0, v[246:247]
	global_load_dwordx4 v[246:249], v[246:247], off offset:256
	v_add_u32_e32 v172, 0x90, v196
	v_ashrrev_i32_e32 v173, 31, v172
	v_lshlrev_b64 v[172:173], 11, v[172:173]
	v_lshl_add_u64 v[172:173], v[198:199], 0, v[172:173]
	global_load_dwordx4 v[172:175], v[172:173], off
	v_pk_mul_f32 v[146:147], v[146:147], v[146:147]
	s_nop 0
	v_pk_fma_f32 v[144:145], v[144:145], v[144:145], v[146:147]
	s_nop 0
	v_pk_fma_f32 v[140:141], v[140:141], v[140:141], v[144:145]
	s_nop 0
	v_pk_fma_f32 v[140:141], v[142:143], v[142:143], v[140:141]
	s_nop 0
	v_pk_fma_f32 v[136:137], v[136:137], v[136:137], v[140:141]
	s_nop 0
	v_pk_fma_f32 v[136:137], v[138:139], v[138:139], v[136:137]
	s_nop 0
	v_pk_fma_f32 v[132:133], v[132:133], v[132:133], v[136:137]
	s_nop 0
	v_pk_fma_f32 v[132:133], v[134:135], v[134:135], v[132:133]
	s_nop 0
	v_add_f32_e32 v132, v132, v133
	v_mov_b32_e32 v133, v132
	s_nop 1
	v_permlane16_swap_b32_e32 v133, v132
	s_waitcnt lgkmcnt(0)
	v_add_f32_e32 v132, v132, v133
	v_mov_b32_e32 v133, v132
	s_nop 1
	v_permlane32_swap_b32_e32 v133, v132
	s_and_saveexec_b64 s[0:1], s[2:3]
	s_cbranch_execz .LBB0_620
	s_waitcnt lgkmcnt(0)
	v_add_f32_e32 v132, v132, v133
	ds_write_b32 v244, v132

; __device__ __forceinline__ unsigned cvt_pk_bf16(float lo, float hi) { unsigned r; asm volatile("v_cvt_pk_bf16_f32 %0, %1, %2" : "=v"(r) : "v"(lo), "v"(hi)); return r; }
; __device__ __forceinline__ float epi_xor16(float v) { return __builtin_bit_cast(float, __builtin_amdgcn_ds_swizzle(__builtin_bit_cast(int, v), (16 << 10) | 0x1f)); }
;     __device__ __forceinline__ void operator()(const f32x4 (&acc)[2][2][4][2], const Unit& u, int wr, int wc, int fr, int fq) const {
;     ...
;             if (ai == 1) {
; #pragma unroll
;                 for (int m = 0; m < 4; ++m)
; #pragma unroll
;                     for (int bj = 0; bj < 2; ++bj) xa[m][bj] = *(const u32x4*)(XB + (size_t)(row0 + HALF + m * 16) * 1024 + col0 + bj * HALF); }
; #pragma unroll
;             for (int m = 0; m < 4; ++m) { const int row = row0 + ai * HALF + m * 16; const float rF = scr[1024 + (row & 255)]; f32x2 s2p = {0.f, 0.f};
; #pragma unroll
;                 for (int bj = 0; bj < 2; ++bj) { const u32x4 xw = xa[m][bj]; float o[8];
; #pragma unroll
;                     for (int n = 0; n < 2; ++n)
; #pragma unroll
;                         for (int e = 0; e < 4; e += 2) { const int q = n * 4 + e; const unsigned w = xw[q >> 1];
;                             const f32x2 xv = {__builtin_bit_cast(float, w << 16), __builtin_bit_cast(float, w & 0xffff0000u)}, av = {acc[ai][bj][m][n][e], acc[ai][bj][m][n][e + 1]}, gv = {gp[bj][q], gp[bj][q + 1]};
;                             const f32x2 ov = xv + av * (gv * rF); s2p += ov * ov; o[q] = ov[0]; o[q + 1] = ov[1]; }
;                     if (OUT) { float* op = OUT + (size_t)row * 1024 + col0 + bj * HALF;
;                         __builtin_nontemporal_store((f32x4){o[0], o[1], o[2], o[3]}, (f32x4*)op); __builtin_nontemporal_store((f32x4){o[4], o[5], o[6], o[7]}, (f32x4*)(op + 4)); }
;                     else { u32x4 w; w.x = cvt_pk_bf16(o[0], o[1]); w.y = cvt_pk_bf16(o[2], o[3]); w.z = cvt_pk_bf16(o[4], o[5]); w.w = cvt_pk_bf16(o[6], o[7]);
;                         *(u32x4*)(XB + (size_t)row * 1024 + col0 + bj * HALF) = w; } }
;                 float s2 = s2p[0] + s2p[1];
;                 s2 += epi_xor16(s2); s2 += epi_xor32(s2, lane);
;                 if (fq == 0) scr[wc * 256 + (row & 255)] = s2; }
.LBB0_626:
	v_add_u32_e32 v164, 0x90, v196
	v_ashrrev_i32_e32 v165, 31, v164
	v_lshlrev_b64 v[164:165], 11, v[164:165]
	v_lshl_add_u64 v[164:165], v[198:199], 0, v[164:165]
	global_load_dwordx4 v[164:167], v[164:165], off offset:256
	v_add_u32_e32 v168, 0xa0, v196
	v_ashrrev_i32_e32 v169, 31, v168
	v_lshlrev_b64 v[168:169], 11, v[168:169]
	v_lshl_add_u64 v[168:169], v[198:199], 0, v[168:169]
	global_load_dwordx4 v[168:171], v[168:169], off
	v_add_u32_e32 v144, 0xa0, v196
	v_ashrrev_i32_e32 v145, 31, v144
	v_lshlrev_b64 v[144:145], 11, v[144:145]
	v_lshl_add_u64 v[144:145], v[198:199], 0, v[144:145]
	global_load_dwordx4 v[144:147], v[144:145], off offset:256
	v_add_u32_e32 v140, 0xb0, v196
	v_ashrrev_i32_e32 v141, 31, v140
	v_lshlrev_b64 v[140:141], 11, v[140:141]
	v_lshl_add_u64 v[140:141], v[198:199], 0, v[140:141]
	global_load_dwordx4 v[140:143], v[140:141], off
	v_pk_mul_f32 v[130:131], v[130:131], v[130:131]
	s_nop 0
	v_pk_fma_f32 v[128:129], v[128:129], v[128:129], v[130:131]
	s_nop 0
	v_pk_fma_f32 v[124:125], v[124:125], v[124:125], v[128:129]
	s_nop 0
	v_pk_fma_f32 v[124:125], v[126:127], v[126:127], v[124:125]
	s_nop 0
	v_pk_fma_f32 v[120:121], v[120:121], v[120:121], v[124:125]
	s_nop 0
	v_pk_fma_f32 v[120:121], v[122:123], v[122:123], v[120:121]
	s_nop 0
	v_pk_fma_f32 v[116:117], v[116:117], v[116:117], v[120:121]
	s_nop 0
	v_pk_fma_f32 v[116:117], v[118:119], v[118:119], v[116:117]
	s_nop 0
	v_add_f32_e32 v116, v116, v117
	v_mov_b32_e32 v117, v116
	s_nop 1
	v_permlane16_swap_b32_e32 v117, v116
	s_waitcnt lgkmcnt(0)
	v_add_f32_e32 v116, v116, v117
	v_mov_b32_e32 v117, v116
	s_nop 1
	v_permlane32_swap_b32_e32 v117, v116
	s_and_saveexec_b64 s[0:1], s[2:3]
	s_cbranch_execz .LBB0_628
	s_waitcnt lgkmcnt(0)
	v_add_f32_e32 v116, v116, v117
	v_lshl_add_u32 v117, v138, 2, s51
	ds_write_b32 v117, v116

; __device__ __forceinline__ unsigned cvt_pk_bf16(float lo, float hi) { unsigned r; asm volatile("v_cvt_pk_bf16_f32 %0, %1, %2" : "=v"(r) : "v"(lo), "v"(hi)); return r; }
; __device__ __forceinline__ float epi_xor16(float v) { return __builtin_bit_cast(float, __builtin_amdgcn_ds_swizzle(__builtin_bit_cast(int, v), (16 << 10) | 0x1f)); }
;     __device__ __forceinline__ void operator()(const f32x4 (&acc)[2][2][4][2], const Unit& u, int wr, int wc, int fr, int fq) const {
;     ...
;             if (ai == 1) {
; #pragma unroll
;                 for (int m = 0; m < 4; ++m)
; #pragma unroll
;                     for (int bj = 0; bj < 2; ++bj) xa[m][bj] = *(const u32x4*)(XB + (size_t)(row0 + HALF + m * 16) * 1024 + col0 + bj * HALF); }
; #pragma unroll
;             for (int m = 0; m < 4; ++m) { const int row = row0 + ai * HALF + m * 16; const float rF = scr[1024 + (row & 255)]; f32x2 s2p = {0.f, 0.f};
; #pragma unroll
;                 for (int bj = 0; bj < 2; ++bj) { const u32x4 xw = xa[m][bj]; float o[8];
; #pragma unroll
;                     for (int n = 0; n < 2; ++n)
; #pragma unroll
;                         for (int e = 0; e < 4; e += 2) { const int q = n * 4 + e; const unsigned w = xw[q >> 1];
;                             const f32x2 xv = {__builtin_bit_cast(float, w << 16), __builtin_bit_cast(float, w & 0xffff0000u)}, av = {acc[ai][bj][m][n][e], acc[ai][bj][m][n][e + 1]}, gv = {gp[bj][q], gp[bj][q + 1]};
;                             const f32x2 ov = xv + av * (gv * rF); s2p += ov * ov; o[q] = ov[0]; o[q + 1] = ov[1]; }
;                     if (OUT) { float* op = OUT + (size_t)row * 1024 + col0 + bj * HALF;
;                         __builtin_nontemporal_store((f32x4){o[0], o[1], o[2], o[3]}, (f32x4*)op); __builtin_nontemporal_store((f32x4){o[4], o[5], o[6], o[7]}, (f32x4*)(op + 4)); }
;                     else { u32x4 w; w.x = cvt_pk_bf16(o[0], o[1]); w.y = cvt_pk_bf16(o[2], o[3]); w.z = cvt_pk_bf16(o[4], o[5]); w.w = cvt_pk_bf16(o[6], o[7]);
;                         *(u32x4*)(XB + (size_t)row * 1024 + col0 + bj * HALF) = w; } }
;                 float s2 = s2p[0] + s2p[1];
;                 s2 += epi_xor16(s2); s2 += epi_xor32(s2, lane);
;                 if (fq == 0) scr[wc * 256 + (row & 255)] = s2; }
.LBB0_634:
	v_add_u32_e32 v156, 0xb0, v196
	v_ashrrev_i32_e32 v157, 31, v156
	v_lshlrev_b64 v[156:157], 11, v[156:157]
	v_lshl_add_u64 v[156:157], v[198:199], 0, v[156:157]
	global_load_dwordx4 v[156:159], v[156:157], off offset:256
	v_pk_mul_f32 v[114:115], v[114:115], v[114:115]
	s_nop 0
	v_pk_fma_f32 v[112:113], v[112:113], v[112:113], v[114:115]
	s_nop 0
	v_pk_fma_f32 v[108:109], v[108:109], v[108:109], v[112:113]
	s_nop 0
	v_pk_fma_f32 v[108:109], v[110:111], v[110:111], v[108:109]
	s_nop 0
	v_pk_fma_f32 v[104:105], v[104:105], v[104:105], v[108:109]
	s_nop 0
	v_pk_fma_f32 v[104:105], v[106:107], v[106:107], v[104:105]
	s_nop 0
	v_pk_fma_f32 v[100:101], v[100:101], v[100:101], v[104:105]
	s_nop 0
	v_pk_fma_f32 v[100:101], v[102:103], v[102:103], v[100:101]
	s_nop 0
	v_add_f32_e32 v100, v100, v101
	v_mov_b32_e32 v101, v100
	s_nop 1
	v_permlane16_swap_b32_e32 v101, v100
	s_waitcnt lgkmcnt(0)
	v_add_f32_e32 v100, v100, v101
	v_mov_b32_e32 v101, v100
	s_nop 1
	v_permlane32_swap_b32_e32 v101, v100
	s_and_saveexec_b64 s[0:1], s[2:3]
	s_cbranch_execz .LBB0_636
	s_waitcnt lgkmcnt(0)
	v_add_f32_e32 v100, v100, v101
	v_lshl_add_u32 v101, v122, 2, s51
	ds_write_b32 v101, v100

;     __device__ __forceinline__ void operator()(const f32x4 (&acc)[2][2][4][2], const Unit& u, int wr, int wc, int fr, int fq) const {
;     ...
;             if (ai == 1) {
; #pragma unroll
;                 for (int m = 0; m < 4; ++m)
; #pragma unroll
;                     for (int bj = 0; bj < 2; ++bj) xa[m][bj] = *(const u32x4*)(XB + (size_t)(row0 + HALF + m * 16) * 1024 + col0 + bj * HALF); }
; #pragma unroll
;             for (int m = 0; m < 4; ++m) { const int row = row0 + ai * HALF + m * 16; const float rF = scr[1024 + (row & 255)]; f32x2 s2p = {0.f, 0.f};
; #pragma unroll
;                 for (int bj = 0; bj < 2; ++bj) { const u32x4 xw = xa[m][bj]; float o[8];
; #pragma unroll
;                     for (int n = 0; n < 2; ++n)
; #pragma unroll
;                         for (int e = 0; e < 4; e += 2) { const int q = n * 4 + e; const unsigned w = xw[q >> 1];
;                             const f32x2 xv = {__builtin_bit_cast(float, w << 16), __builtin_bit_cast(float, w & 0xffff0000u)}, av = {acc[ai][bj][m][n][e], acc[ai][bj][m][n][e + 1]}, gv = {gp[bj][q], gp[bj][q + 1]};
;                             const f32x2 ov = xv + av * (gv * rF); s2p += ov * ov; o[q] = ov[0]; o[q + 1] = ov[1]; }
.LBB0_644:
	s_or_b64 exec, exec, s[0:1]
	v_add_u32_e32 v128, 0x80, v196
	v_add_u32_e32 v122, 0x90, v196
	v_ashrrev_i32_e32 v129, 31, v128
	v_ashrrev_i32_e32 v123, 31, v122
	v_add_u32_e32 v118, 0xa0, v196
	v_lshlrev_b64 v[124:125], 11, v[128:129]
	v_lshlrev_b64 v[120:121], 11, v[122:123]
	v_ashrrev_i32_e32 v119, 31, v118
	v_add_u32_e32 v114, 0xb0, v196
	v_lshl_add_u64 v[126:127], v[198:199], 0, v[124:125]
	s_waitcnt lgkmcnt(0)
	v_lshl_add_u64 v[84:85], v[198:199], 0, v[120:121]
	v_lshlrev_b64 v[116:117], 11, v[118:119]
	v_ashrrev_i32_e32 v115, 31, v114
	v_lshl_add_u64 v[84:85], v[198:199], 0, v[116:117]
	v_lshlrev_b64 v[112:113], 11, v[114:115]
	v_lshl_add_u64 v[84:85], v[198:199], 0, v[112:113]
	s_nop 0
	s_nop 0
	s_waitcnt vmcnt(2)
	v_mov_b64_e32 v[132:133], v[200:201]
	v_mov_b64_e32 v[134:135], v[202:203]
	v_mov_b64_e32 v[108:109], v[246:247]
	v_mov_b64_e32 v[110:111], v[248:249]
	v_mov_b64_e32 v[104:105], v[172:173]
	v_mov_b64_e32 v[106:107], v[174:175]
	v_mov_b64_e32 v[100:101], v[164:165]
	v_mov_b64_e32 v[102:103], v[166:167]
	v_mov_b64_e32 v[96:97], v[168:169]
	v_mov_b64_e32 v[98:99], v[170:171]
	v_mov_b64_e32 v[92:93], v[144:145]
	v_mov_b64_e32 v[94:95], v[146:147]
	v_mov_b64_e32 v[88:89], v[140:141]
	v_mov_b64_e32 v[90:91], v[142:143]
	v_mov_b64_e32 v[84:85], v[156:157]
	v_mov_b64_e32 v[86:87], v[158:159]
	v_and_b32_e32 v130, 0xcf, v128
	v_lshl_add_u32 v126, v130, 2, s93
	ds_read_b32 v126, v126 offset:4096
	v_lshlrev_b64 v[128:129], 12, v[128:129]
	v_lshl_add_u64 v[128:129], s[10:11], 0, v[128:129]
	s_and_b64 vcc, exec, s[8:9]
	v_lshl_add_u64 v[128:129], v[192:193], 2, v[128:129]
	s_waitcnt lgkmcnt(0)
	v_pk_mul_f32 v[138:139], v[80:81], v[126:127] op_sel_hi:[1,0]
	v_lshlrev_b32_e32 v136, 16, v132
	v_and_b32_e32 v137, 0xffff0000, v132
	v_pk_fma_f32 v[72:73], v[72:73], v[138:139], v[136:137]
	v_lshlrev_b32_e32 v132, 16, v133
	v_and_b32_e32 v133, 0xffff0000, v133
	v_pk_mul_f32 v[136:137], v[82:83], v[126:127] op_sel_hi:[1,0]
	s_nop 0
	v_pk_fma_f32 v[74:75], v[74:75], v[136:137], v[132:133]
	v_lshlrev_b32_e32 v132, 16, v134
	v_and_b32_e32 v133, 0xffff0000, v134
	v_pk_mul_f32 v[136:137], v[76:77], v[126:127] op_sel_hi:[1,0]
	s_nop 0
	v_pk_fma_f32 v[64:65], v[64:65], v[136:137], v[132:133]
	v_lshlrev_b32_e32 v132, 16, v135
	v_and_b32_e32 v133, 0xffff0000, v135
	v_pk_mul_f32 v[134:135], v[78:79], v[126:127] op_sel_hi:[1,0]
	s_nop 0
	v_pk_fma_f32 v[66:67], v[66:67], v[134:135], v[132:133]
	s_cbranch_vccnz .LBB0_689
	global_store_dwordx4 v[128:129], v[72:75], off nt
	global_store_dwordx4 v[128:129], v[64:67], off offset:16 nt
	v_lshl_add_u64 v[124:125], s[54:55], 0, v[124:125]
	v_lshl_add_u64 v[124:125], v[192:193], 1, v[124:125]
	s_cbranch_execnz .LBB0_647
